# baseline (speedup 1.0000x reference)
.LBB1_52:
	s_or_b64 exec, exec, s[8:9]
	v_lshlrev_b32_e32 v1, 1, v0
	s_movk_i32 s8, 0xc4
	v_cmp_gt_u32_e64 s[10:11], s8, v0
	v_mov_b32_e32 v53, 0
	v_lshlrev_b32_e32 v56, 2, v1
	v_mov_b32_e32 v55, 0
	s_waitcnt lgkmcnt(0)
	s_barrier
	s_and_saveexec_b64 s[8:9], s[10:11]
	ds_read_b32 v55, v56 offset:4160
	s_or_b64 exec, exec, s[8:9]
	v_or_b32_e32 v54, 1, v1
	s_movk_i32 s8, 0x187
	v_cmp_gt_u32_e64 s[8:9], s8, v54
	s_and_saveexec_b64 s[12:13], s[8:9]
	ds_read_b32 v53, v56 offset:4164
	s_or_b64 exec, exec, s[12:13]
	s_waitcnt lgkmcnt(0)
	v_add_u32_e32 v56, v53, v55
	v_mov_b32_e32 v57, v56
	v_lshrrev_b32_e32 v59, 6, v0
	v_and_b32_e32 v58, 63, v0
	v_add_u32_dpp v57, v57, v57 row_shr:1 row_mask:0xf bank_mask:0xf bound_ctrl:1
	s_nop 1
	v_add_u32_dpp v57, v57, v57 row_shr:2 row_mask:0xf bank_mask:0xf bound_ctrl:1
	s_nop 1
	v_add_u32_dpp v57, v57, v57 row_shr:4 row_mask:0xf bank_mask:0xf bound_ctrl:1
	s_nop 1
	v_add_u32_dpp v57, v57, v57 row_shr:8 row_mask:0xf bank_mask:0xf bound_ctrl:1
	s_nop 1
	v_add_u32_dpp v57, v57, v57 row_bcast:15 row_mask:0xa bank_mask:0xf
	s_nop 1
	v_add_u32_dpp v57, v57, v57 row_bcast:31 row_mask:0xc bank_mask:0xf
	v_cmp_eq_u32_e64 s[12:13], 63, v58
	v_lshlrev_b32_e32 v58, 2, v59
	s_and_saveexec_b64 s[14:15], s[12:13]
	ds_write_b32 v58, v57
	s_mov_b64 exec, s[14:15]
	s_waitcnt lgkmcnt(0)
	s_barrier
	v_mov_b32_e32 v58, 0
	ds_read_b128 v[60:63], v58
	v_cmp_lt_u32_e64 s[36:37], 0, v59
	v_cmp_lt_u32_e64 s[12:13], 1, v59
	v_cmp_lt_u32_e64 s[14:15], 2, v59
	s_waitcnt lgkmcnt(0)
	v_cndmask_b32_e64 v60, 0, v60, s[36:37]
	v_cndmask_b32_e64 v61, 0, v61, s[12:13]
	v_cndmask_b32_e64 v62, 0, v62, s[14:15]
	v_add3_u32 v57, v57, v60, v61
	v_add_u32_e32 v57, v57, v62
	v_add_u32_e32 v40, v40, v34
	v_sub_u32_e32 v56, v57, v56
	s_and_saveexec_b64 s[12:13], s[10:11]
	s_cbranch_execz .LBB1_80
	v_mov_b32_e32 v60, v55
	v_mov_b32_e32 v61, v53
	v_lshlrev_b32_e32 v57, 8, v0
	global_atomic_add_x2 v[62:63], v57, v[60:61], s[16:17] sc0
	ds_write_b32 v40, v56 offset:1024
	v_add_u32_e32 v58, v56, v55
	s_and_saveexec_b64 s[14:15], s[8:9]
	ds_write_b32 v40, v58 offset:1028
	s_or_b64 exec, exec, s[14:15]
	s_waitcnt vmcnt(0)
	ds_write_b32 v40, v62 offset:2592
	s_and_saveexec_b64 s[14:15], s[8:9]
	ds_write_b32 v40, v63 offset:2596

.LBB2_27:
	s_or_b64 exec, exec, s[4:5]
	v_lshlrev_b32_e32 v8, 2, v0
	s_waitcnt vmcnt(0)
	v_add_u32_e32 v4, v4, v1
	v_mov_b32_e32 v5, v4
	v_lshrrev_b32_e32 v70, 6, v0
	v_and_b32_e32 v71, 63, v0
	v_add_u32_dpp v5, v5, v5 row_shr:1 row_mask:0xf bank_mask:0xf bound_ctrl:1
	s_nop 1
	v_add_u32_dpp v5, v5, v5 row_shr:2 row_mask:0xf bank_mask:0xf bound_ctrl:1
	s_nop 1
	v_add_u32_dpp v5, v5, v5 row_shr:4 row_mask:0xf bank_mask:0xf bound_ctrl:1
	s_nop 1
	v_add_u32_dpp v5, v5, v5 row_shr:8 row_mask:0xf bank_mask:0xf bound_ctrl:1
	s_nop 1
	v_add_u32_dpp v5, v5, v5 row_bcast:15 row_mask:0xa bank_mask:0xf
	s_nop 1
	v_add_u32_dpp v5, v5, v5 row_bcast:31 row_mask:0xc bank_mask:0xf
	v_cmp_eq_u32_e32 vcc, 63, v71
	v_lshlrev_b32_e32 v71, 2, v70
	s_and_saveexec_b64 s[4:5], vcc
	ds_write_b32 v71, v5
	s_mov_b64 exec, s[4:5]
	s_load_dwordx2 s[10:11], s[0:1], 0x0
	s_waitcnt lgkmcnt(0)
	s_barrier
	v_mov_b32_e32 v71, 0
	ds_read_b128 v[72:75], v71
	v_cmp_lt_u32_e32 vcc, 0, v70
	v_cmp_lt_u32_e64 s[4:5], 1, v70
	v_cmp_lt_u32_e64 s[6:7], 2, v70
	s_waitcnt lgkmcnt(0)
	v_cndmask_b32_e32 v72, 0, v72, vcc
	v_cndmask_b32_e64 v73, 0, v73, s[4:5]
	v_cndmask_b32_e64 v74, 0, v74, s[6:7]
	v_add3_u32 v5, v5, v72, v73
	v_add_u32_e32 v5, v5, v74
	v_cmp_eq_u32_e64 s[6:7], s2, v2
	v_cmp_eq_u32_e64 s[4:5], s2, v3
	s_or_b64 s[12:13], s[6:7], s[4:5]
	s_and_saveexec_b64 s[6:7], s[12:13]
	v_cndmask_b32_e64 v1, 0, v1, s[4:5]
	v_sub_u32_e32 v1, v1, v4
	v_add_u32_e32 v1, v1, v5
	v_mov_b32_e32 v2, 0
	ds_write_b32 v2, v1 offset:2048
	s_or_b64 exec, exec, s[6:7]
	s_lshr_b32 s80, s2, 1
	s_lshl_b32 s80, s80, 6
	s_and_b32 s81, s2, 1
	s_or_b32 s80, s80, s81
	s_mov_b32 s81, 0
	s_lshl_b64 s[4:5], s[80:81], 2
	s_add_u32 s4, s8, s4
	v_mov_b32_e32 v1, 0
	s_addc_u32 s5, s9, s5
	ds_write_b32 v8, v1 offset:1024
	s_waitcnt lgkmcnt(0)
	s_barrier
	s_load_dword s3, s[4:5], 0x0
	ds_read_b32 v2, v1 offset:2048
	s_waitcnt lgkmcnt(0)
	s_cmpk_lt_i32 s3, 0x1801
	s_cbranch_scc1 .LBB2_47
	s_load_dword s81, s[8:9], 0xc380

.LBB2_124:
	s_or_b64 exec, exec, s[76:77]
	s_load_dwordx4 s[76:79], s[0:1], 0x28
	s_waitcnt lgkmcnt(0)
	s_barrier
	ds_read_b32 v6, v8 offset:1024
	s_waitcnt lgkmcnt(0)
	v_mov_b32_e32 v7, v6
	v_lshrrev_b32_e32 v70, 6, v0
	v_and_b32_e32 v71, 63, v0
	v_add_u32_dpp v7, v7, v7 row_shr:1 row_mask:0xf bank_mask:0xf bound_ctrl:1
	s_nop 1
	v_add_u32_dpp v7, v7, v7 row_shr:2 row_mask:0xf bank_mask:0xf bound_ctrl:1
	s_nop 1
	v_add_u32_dpp v7, v7, v7 row_shr:4 row_mask:0xf bank_mask:0xf bound_ctrl:1
	s_nop 1
	v_add_u32_dpp v7, v7, v7 row_shr:8 row_mask:0xf bank_mask:0xf bound_ctrl:1
	s_nop 1
	v_add_u32_dpp v7, v7, v7 row_bcast:15 row_mask:0xa bank_mask:0xf
	s_nop 1
	v_add_u32_dpp v7, v7, v7 row_bcast:31 row_mask:0xc bank_mask:0xf
	v_cmp_eq_u32_e32 vcc, 63, v71
	v_lshlrev_b32_e32 v71, 2, v70
	s_and_saveexec_b64 s[0:1], vcc
	ds_write_b32 v71, v7
	s_mov_b64 exec, s[0:1]
	s_lshl_b32 s33, s2, 8
	s_waitcnt lgkmcnt(0)
	s_barrier
	v_mov_b32_e32 v71, 0
	ds_read_b128 v[72:75], v71
	v_cmp_lt_u32_e32 vcc, 0, v70
	v_cmp_lt_u32_e64 s[52:53], 1, v70
	v_cmp_lt_u32_e64 s[54:55], 2, v70
	s_waitcnt lgkmcnt(0)
	v_cndmask_b32_e32 v72, 0, v72, vcc
	v_cndmask_b32_e64 v73, 0, v73, s[52:53]
	v_cndmask_b32_e64 v74, 0, v74, s[54:55]
	v_add3_u32 v7, v7, v72, v73
	v_add_u32_e32 v7, v7, v74
	s_mov_b32 s0, 0x186a0
	v_or_b32_e32 v4, s33, v0
	v_cmp_lt_u32_e32 vcc, s0, v4
	v_sub_u32_e32 v51, v7, v6
	v_add_u32_e32 v52, v51, v2
	s_and_saveexec_b64 s[0:1], vcc
	s_xor_b64 s[0:1], exec, s[0:1]
	v_add_u32_e32 v52, v51, v2
	s_andn2_saveexec_b64 s[0:1], s[0:1]
	s_cbranch_execz .LBB2_144
	v_mov_b32_e32 v5, 0
	v_lshl_add_u64 v[4:5], v[4:5], 2, s[72:73]
	global_store_dword v[4:5], v52, off
